# plus cache-warming prefetch of the later iterations' q/k rows ahead of the chunk-A causal-conv loop
# speedup vs baseline: 1.0052x; 1.0052x over previous
.LBB0_625:
	s_waitcnt lgkmcnt(0)
	s_barrier
	s_and_saveexec_b64 s[62:63], s[44:45]
	s_cbranch_execz .LBB0_641
	s_lshl_b32 s4, s96, 7
	s_lshl_b32 s21, s96, 8
	s_add_u32 s68, s2, s21
	s_addc_u32 s69, s82, 0
	s_cmp_gt_i32 s95, -1
	s_mov_b64 s[70:71], 0
	s_cselect_b64 s[72:73], -1, 0
	v_mov_b32_e32 v16, v33
	v_mov_b32_e32 v17, v32
	v_and_b32_e32 v212, 0x78, v16
	v_or_b32_e32 v212, s4, v212
	v_lshlrev_b32_e32 v210, 1, v212
	v_mov_b32_e32 v211, 0
	v_lshl_add_u64 v[208:209], s[10:11], 0, v[210:211]
	v_bfe_u32 v213, v17, 4, 6
	v_or_b32_e32 v213, s66, v213
	v_add_u32_e32 v214, 29, v213
	v_max_i32_e32 v214, 0, v214
	v_mad_u64_u32 v[210:211], vcc, v214, s83, v[208:209]
	global_load_dwordx4 v[204:207], v[210:211], off
	v_add_u32_e32 v214, 30, v213
	v_max_i32_e32 v214, 0, v214
	v_mad_u64_u32 v[210:211], vcc, v214, s83, v[208:209]
	global_load_dwordx4 v[204:207], v[210:211], off
	v_add_u32_e32 v214, 31, v213
	v_max_i32_e32 v214, 0, v214
	v_mad_u64_u32 v[210:211], vcc, v214, s83, v[208:209]
	global_load_dwordx4 v[204:207], v[210:211], off
	v_add_u32_e32 v214, 32, v213
	v_max_i32_e32 v214, 0, v214
	v_mad_u64_u32 v[210:211], vcc, v214, s83, v[208:209]
	global_load_dwordx4 v[204:207], v[210:211], off
	v_add_u32_e32 v214, 0xfffffffd, v213
	v_max_i32_e32 v214, 0, v214
	v_mad_u64_u32 v[210:211], vcc, v214, s83, v[208:209]
	global_load_dwordx4 v[204:207], v[210:211], off offset:1024
	v_add_u32_e32 v214, 0xfffffffe, v213
	v_max_i32_e32 v214, 0, v214
	v_mad_u64_u32 v[210:211], vcc, v214, s83, v[208:209]
	global_load_dwordx4 v[204:207], v[210:211], off offset:1024
	v_add_u32_e32 v214, 0xffffffff, v213
	v_max_i32_e32 v214, 0, v214
	v_mad_u64_u32 v[210:211], vcc, v214, s83, v[208:209]
	global_load_dwordx4 v[204:207], v[210:211], off offset:1024
	v_add_u32_e32 v214, 0, v213
	v_max_i32_e32 v214, 0, v214
	v_mad_u64_u32 v[210:211], vcc, v214, s83, v[208:209]
	global_load_dwordx4 v[204:207], v[210:211], off offset:1024
	v_add_u32_e32 v214, 29, v213
	v_max_i32_e32 v214, 0, v214
	v_mad_u64_u32 v[210:211], vcc, v214, s83, v[208:209]
	global_load_dwordx4 v[204:207], v[210:211], off offset:1024
	v_add_u32_e32 v214, 30, v213
	v_max_i32_e32 v214, 0, v214
	v_mad_u64_u32 v[210:211], vcc, v214, s83, v[208:209]
	global_load_dwordx4 v[204:207], v[210:211], off offset:1024
	v_add_u32_e32 v214, 31, v213
	v_max_i32_e32 v214, 0, v214
	v_mad_u64_u32 v[210:211], vcc, v214, s83, v[208:209]
	global_load_dwordx4 v[204:207], v[210:211], off offset:1024
	v_add_u32_e32 v214, 32, v213
	v_max_i32_e32 v214, 0, v214
	v_mad_u64_u32 v[210:211], vcc, v214, s83, v[208:209]
	global_load_dwordx4 v[204:207], v[210:211], off offset:1024
	s_branch .LBB0_628
